# P0 rms-norm loop: loop-invariant g_mix loads hoisted out of the row loop (one round trip per row instead of eight)
# baseline (speedup 1.0000x reference)
; __device__ __forceinline__ unsigned cvt_pk_bf16(float lo, float hi) { unsigned r; asm volatile("v_cvt_pk_bf16_f32 %0, %1, %2" : "=v"(r) : "v"(lo), "v"(hi)); return r; }
; __device__ __forceinline__ unsigned cvt_pk4_fp8(float a, float b, float c, float d) { int w; asm("" : "=v"(w));     w = __builtin_amdgcn_cvt_pk_fp8_f32(a, b, w, false); w = __builtin_amdgcn_cvt_pk_fp8_f32(c, d, w, true); return (unsigned)w; }
; __device__ __forceinline__ float wave_sum(float v) {
; #pragma unroll
;     for (int o = 1; o < 64; o <<= 1) v += __shfl_xor(v, o);
;     return v;
; __global__ void __launch_bounds__(512, 2) fwd_kernel(Params p) {
;     ...
;         for (int m = gw; m < T; m += NGW) {
;             const f32x4* xr = (const f32x4*)(p.in[I_X] + (size_t)m * DM) + lane; const f32x4* gr = (const f32x4*)p.in[I_GMIX] + lane;
;             f32x4 v[8]; float s = 0.f;
; #pragma unroll
;             for (int j = 0; j < 8; ++j) { v[j] = xr[64 * j]; s += (v[j].x * v[j].x + v[j].y * v[j].y) + (v[j].z * v[j].z + v[j].w * v[j].w); }
;             const float rstd = rsqrtf(wave_sum(s) * (1.f / DM) + RMS_EPS);
;             u32x2* o8 = (u32x2*)(Hb + (size_t)m * DM) + lane; unsigned* o4 = (unsigned*)(H8 + (size_t)m * DM) + lane;
; #pragma unroll
;             for (int j = 0; j < 8; ++j) { const f32x4 g = gr[64 * j]; const f32x4 hv = v[j] * rstd * g; u32x2 w; w.x = cvt_pk_bf16(hv.x, hv.y); w.y = cvt_pk_bf16(hv.z, hv.w); o8[64 * j] = w; o4[64 * j] = cvt_pk4_fp8(hv.x, hv.y, hv.z, hv.w); }
.LBB0_44:
	s_or_b64 exec, exec, s[8:9]
	s_cmpk_gt_i32 s16, 0x3fff
	v_mbcnt_lo_u32_b32 v138, -1, 0
	s_cbranch_scc1 .LBB0_47
	v_mbcnt_hi_u32_b32 v2, -1, v138
	v_and_b32_e32 v3, 64, v2
	v_add_u32_e32 v3, 64, v3
	v_xor_b32_e32 v4, 1, v2
	v_cmp_lt_i32_e32 vcc, v4, v3
	s_load_dwordx2 s[0:1], s[88:89], 0x10
	s_load_dwordx2 s[4:5], s[88:89], 0x0
	v_cndmask_b32_e32 v4, v2, v4, vcc
	v_lshlrev_b32_e32 v32, 2, v4
	v_xor_b32_e32 v4, 2, v2
	v_cmp_lt_i32_e32 vcc, v4, v3
	v_ashrrev_i32_e32 v21, 31, v20
	s_ashr_i32 s17, s16, 31
	v_cndmask_b32_e32 v4, v2, v4, vcc
	v_lshlrev_b32_e32 v33, 2, v4
	v_xor_b32_e32 v4, 4, v2
	v_cmp_lt_i32_e32 vcc, v4, v3
	v_lshlrev_b64 v[0:1], 4, v[20:21]
	s_lshl_b64 s[6:7], s[16:17], 11
	v_cndmask_b32_e32 v4, v2, v4, vcc
	v_lshlrev_b32_e32 v34, 2, v4
	v_xor_b32_e32 v4, 8, v2
	v_cmp_lt_i32_e32 vcc, v4, v3
	s_ashr_i32 s19, s18, 31
	s_lshl_b64 s[8:9], s[16:17], 12
	v_cndmask_b32_e32 v4, v2, v4, vcc
	v_lshlrev_b32_e32 v35, 2, v4
	v_xor_b32_e32 v4, 16, v2
	v_cmp_lt_i32_e32 vcc, v4, v3
	s_waitcnt lgkmcnt(0)
	v_lshl_add_u64 v[16:17], s[0:1], 0, v[0:1]
	s_mov_b64 s[0:1], 0x1000
	v_cndmask_b32_e32 v4, v2, v4, vcc
	v_lshl_add_u64 v[28:29], v[20:21], 2, s[6:7]
	s_lshl_b64 s[6:7], s[18:19], 11
	v_lshl_add_u64 v[20:21], v[20:21], 3, s[8:9]
	s_lshl_b64 s[8:9], s[18:19], 12
	s_lshl_b64 s[10:11], s[16:17], 13
	v_lshlrev_b32_e32 v36, 2, v4
	v_xor_b32_e32 v4, 32, v2
	v_lshl_add_u64 v[18:19], v[16:17], 0, s[0:1]
	s_mov_b64 s[0:1], 0x1400
	s_add_u32 s4, s4, s10
	v_cmp_lt_i32_e32 vcc, v4, v3
	v_lshl_add_u64 v[22:23], v[16:17], 0, s[0:1]
	s_mov_b64 s[0:1], 0x1800
	s_addc_u32 s5, s5, s11
	v_cndmask_b32_e32 v2, v2, v4, vcc
	v_lshl_add_u64 v[24:25], v[16:17], 0, s[0:1]
	s_mov_b64 s[0:1], 0x1c00
	v_lshl_add_u64 v[0:1], s[4:5], 0, v[0:1]
	v_lshlrev_b32_e32 v37, 2, v2
	v_lshl_add_u64 v[26:27], v[16:17], 0, s[0:1]
	v_lshl_add_u64 v[30:31], v[0:1], 0, s[0:1]
	s_lshl_b64 s[10:11], s[18:19], 13
	v_mov_b32_e32 v38, 0x358637bd
	s_mov_b32 s0, 0x800000
	s_mov_b32 s1, 0x7800000
	s_brev_b32 s3, 37
	s_mov_b32 s12, s16
	global_load_dwordx4 v[56:59], v[16:17], off
	global_load_dwordx4 v[100:103], v[16:17], off offset:1024
	global_load_dwordx4 v[104:107], v[16:17], off offset:2048
	global_load_dwordx4 v[108:111], v[16:17], off offset:3072
	global_load_dwordx4 v[112:115], v[18:19], off
	global_load_dwordx4 v[116:119], v[22:23], off
	global_load_dwordx4 v[120:123], v[24:25], off
	global_load_dwordx4 v[124:127], v[26:27], off
.LBB0_46:
	v_add_co_u32_e32 v60, vcc, 0xfffff000, v30
	global_load_dwordx4 v[12:15], v[30:31], off offset:-3072
	global_load_dwordx4 v[8:11], v[30:31], off offset:-2048
	global_load_dwordx4 v[4:7], v[30:31], off offset:-1024
	v_addc_co_u32_e32 v61, vcc, -1, v31, vcc
	global_load_dwordx4 v[40:43], v[60:61], off offset:-3072
	global_load_dwordx4 v[44:47], v[60:61], off offset:-2048
	global_load_dwordx4 v[48:51], v[60:61], off offset:-1024
	global_load_dwordx4 v[52:55], v[30:31], off offset:-4096
	global_load_dwordx4 v[0:3], v[30:31], off
	s_add_i32 s12, s12, s18
	s_cmpk_gt_i32 s12, 0x3fff
	v_lshl_add_u64 v[30:31], v[30:31], 0, s[10:11]
	s_waitcnt vmcnt(4)
	v_mov_b32_e32 v70, v41
	v_pk_mul_f32 v[60:61], v[10:11], v[10:11]
	v_pk_mul_f32 v[62:63], v[8:9], v[8:9]
	v_mul_f32_e32 v64, v5, v5
	v_mul_f32_e32 v66, v7, v7
	s_waitcnt vmcnt(0)
	v_mul_f32_e32 v81, v2, v2
	v_mul_f32_e32 v88, v3, v3
	v_pk_mov_b32 v[68:69], v[62:63], v[60:61] op_sel:[1,0]
	v_mov_b32_e32 v63, v61
	v_pk_fma_f32 v[60:61], v[4:5], v[4:5], v[64:65] op_sel_hi:[1,1,0]
	v_pk_fma_f32 v[64:65], v[6:7], v[6:7], v[66:67] op_sel_hi:[1,1,0]
	v_mov_b32_e32 v71, v45
	v_mov_b32_e32 v74, v43
	v_mov_b32_e32 v75, v47
	v_mov_b32_e32 v66, v40
	v_mov_b32_e32 v67, v44
	v_mov_b32_e32 v72, v42
	v_mov_b32_e32 v73, v46
	v_pk_mul_f32 v[76:77], v[50:51], v[50:51]
	v_pk_mul_f32 v[78:79], v[48:49], v[48:49]
	v_pk_add_f32 v[62:63], v[68:69], v[62:63]
	v_mov_b32_e32 v61, v81
	v_mov_b32_e32 v65, v88
	v_pk_mul_f32 v[68:69], v[70:71], v[70:71]
	v_pk_mul_f32 v[70:71], v[74:75], v[74:75]
	v_pk_mov_b32 v[74:75], v[78:79], v[76:77] op_sel:[1,0]
	v_mov_b32_e32 v79, v77
	v_pk_add_f32 v[60:61], v[60:61], v[64:65]
	v_pk_fma_f32 v[64:65], v[66:67], v[66:67], v[68:69]
	v_pk_fma_f32 v[66:67], v[72:73], v[72:73], v[70:71]
	v_mul_f32_e32 v83, v13, v13
	v_mul_f32_e32 v80, v53, v53
	v_mul_f32_e32 v82, v55, v55
	v_pk_add_f32 v[68:69], v[74:75], v[78:79]
	v_pk_add_f32 v[64:65], v[64:65], v[66:67]
	v_mul_f32_e32 v39, v12, v12
	v_mul_f32_e32 v84, v14, v14
	v_mul_f32_e32 v85, v15, v15
	v_pk_fma_f32 v[76:77], v[52:53], v[52:53], v[80:81] op_sel_hi:[1,1,0]
	v_pk_fma_f32 v[80:81], v[54:55], v[54:55], v[82:83] op_sel_hi:[1,1,0]
	v_pk_add_f32 v[66:67], v[68:69], v[68:69] op_sel:[0,1] op_sel_hi:[1,0]
	v_pk_add_f32 v[64:65], v[64:65], v[64:65] op_sel:[0,1] op_sel_hi:[1,0]
	v_mov_b32_e32 v77, v84
	v_mov_b32_e32 v81, v85
	v_mov_b32_e32 v67, v83
	v_mov_b32_e32 v65, v39
	v_pk_add_f32 v[68:69], v[76:77], v[80:81]
	v_pk_add_f32 v[64:65], v[64:65], v[66:67]
	v_mul_f32_e32 v86, v0, v0
	v_pk_add_f32 v[64:65], v[64:65], v[68:69]
	v_mul_f32_e32 v87, v1, v1
	v_pk_add_f32 v[62:63], v[62:63], v[62:63] op_sel:[0,1] op_sel_hi:[1,0]
	v_pk_add_f32 v[64:65], v[64:65], v[64:65] op_sel:[0,1] op_sel_hi:[1,0]
	v_mov_b32_e32 v63, v87
	v_mov_b32_e32 v65, v86
	v_pk_add_f32 v[62:63], v[64:65], v[62:63]
	s_nop 0
	v_pk_add_f32 v[60:61], v[62:63], v[60:61]
	v_add_f32_e32 v39, v60, v61
	ds_bpermute_b32 v60, v32, v39
	s_waitcnt lgkmcnt(0)
; __device__ __forceinline__ unsigned cvt_pk_bf16(float lo, float hi) { unsigned r; asm volatile("v_cvt_pk_bf16_f32 %0, %1, %2" : "=v"(r) : "v"(lo), "v"(hi)); return r; }
; __device__ __forceinline__ unsigned cvt_pk4_fp8(float a, float b, float c, float d) { int w; asm("" : "=v"(w));     w = __builtin_amdgcn_cvt_pk_fp8_f32(a, b, w, false); w = __builtin_amdgcn_cvt_pk_fp8_f32(c, d, w, true); return (unsigned)w; }
; __device__ __forceinline__ float wave_sum(float v) {
; #pragma unroll
;     for (int o = 1; o < 64; o <<= 1) v += __shfl_xor(v, o);
;     return v;
; __global__ void __launch_bounds__(512, 2) fwd_kernel(Params p) {
;     ...
;             const float rstd = rsqrtf(wave_sum(s) * (1.f / DM) + RMS_EPS);
;             u32x2* o8 = (u32x2*)(Hb + (size_t)m * DM) + lane; unsigned* o4 = (unsigned*)(H8 + (size_t)m * DM) + lane;
; #pragma unroll
;             for (int j = 0; j < 8; ++j) { const f32x4 g = gr[64 * j]; const f32x4 hv = v[j] * rstd * g; u32x2 w; w.x = cvt_pk_bf16(hv.x, hv.y); w.y = cvt_pk_bf16(hv.z, hv.w); o8[64 * j] = w; o4[64 * j] = cvt_pk4_fp8(hv.x, hv.y, hv.z, hv.w); }
	v_add_f32_e32 v39, v39, v60
	ds_bpermute_b32 v60, v33, v39
	s_waitcnt lgkmcnt(0)
	v_add_f32_e32 v39, v39, v60
	ds_bpermute_b32 v62, v34, v39
	v_lshl_add_u64 v[60:61], s[28:29], 0, v[20:21]
	v_add_co_u32_e32 v60, vcc, s1, v60
	v_lshl_add_u64 v[20:21], v[20:21], 0, s[8:9]
	s_waitcnt lgkmcnt(0)
	v_add_f32_e32 v39, v39, v62
	ds_bpermute_b32 v64, v35, v39
	v_addc_co_u32_e32 v61, vcc, 0, v61, vcc
	v_lshl_add_u64 v[62:63], s[28:29], 0, v[28:29]
	v_add_co_u32_e64 v62, s[4:5], s3, v62
	s_waitcnt lgkmcnt(0)
	v_add_f32_e32 v39, v39, v64
	ds_bpermute_b32 v64, v36, v39
	v_lshl_add_u64 v[28:29], v[28:29], 0, s[6:7]
	s_waitcnt lgkmcnt(0)
	v_add_f32_e32 v39, v39, v64
	ds_bpermute_b32 v64, v37, v39
	s_waitcnt lgkmcnt(0)
	v_add_f32_e32 v39, v39, v64
	v_fmamk_f32 v39, v39, 0x3a000000, v38
	v_mul_f32_e32 v64, 0x4b800000, v39
	v_cmp_gt_f32_e32 vcc, s0, v39
	s_nop 1
	v_cndmask_b32_e32 v39, v39, v64, vcc
	v_rsq_f32_e32 v39, v39
	s_nop 0
	v_mul_f32_e32 v64, 0x45800000, v39
	v_cndmask_b32_e32 v64, v39, v64, vcc
	v_pk_mul_f32 v[40:41], v[64:65], v[40:41] op_sel_hi:[0,1]
	s_waitcnt vmcnt(0)
	v_pk_mul_f32 v[40:41], v[56:57], v[40:41]
	v_pk_mul_f32 v[42:43], v[64:65], v[42:43] op_sel_hi:[0,1]
	v_cvt_pk_fp8_f32 v66, v40, v41
	v_pk_mul_f32 v[42:43], v[58:59], v[42:43]
	v_cvt_pk_bf16_f32 v40, v40, v41
	v_addc_co_u32_e64 v63, vcc, 0, v63, s[4:5]
	v_cvt_pk_fp8_f32 v66, v42, v43 op_sel:[0,0,1]
	v_cvt_pk_bf16_f32 v41, v42, v43
	global_store_dwordx2 v[60:61], v[40:41], off
	global_store_dword v[62:63], v66, off
	v_pk_mul_f32 v[44:45], v[64:65], v[44:45] op_sel_hi:[0,1]
	v_pk_mul_f32 v[12:13], v[64:65], v[12:13] op_sel_hi:[0,1]
	v_pk_mul_f32 v[14:15], v[64:65], v[14:15] op_sel_hi:[0,1]
	v_pk_mul_f32 v[8:9], v[64:65], v[8:9] op_sel_hi:[0,1]
	v_pk_mul_f32 v[10:11], v[64:65], v[10:11] op_sel_hi:[0,1]
	v_pk_mul_f32 v[4:5], v[64:65], v[4:5] op_sel_hi:[0,1]
	v_pk_mul_f32 v[6:7], v[64:65], v[6:7] op_sel_hi:[0,1]
	v_pk_mul_f32 v[0:1], v[64:65], v[0:1] op_sel_hi:[0,1]
	v_pk_mul_f32 v[40:41], v[100:101], v[44:45]
	s_nop 0
	v_cvt_pk_fp8_f32 v39, v40, v41
	v_pk_mul_f32 v[44:45], v[64:65], v[46:47] op_sel_hi:[0,1]
	v_pk_mul_f32 v[42:43], v[102:103], v[44:45]
	v_cvt_pk_bf16_f32 v40, v40, v41
	v_pk_mul_f32 v[44:45], v[64:65], v[48:49] op_sel_hi:[0,1]
	v_cvt_pk_fp8_f32 v39, v42, v43 op_sel:[0,0,1]
	v_cvt_pk_bf16_f32 v41, v42, v43
	global_store_dwordx2 v[60:61], v[40:41], off offset:512
	global_store_dword v[62:63], v39, off offset:256
	v_pk_mul_f32 v[40:41], v[104:105], v[44:45]
	s_nop 0
	v_cvt_pk_fp8_f32 v39, v40, v41
	v_pk_mul_f32 v[44:45], v[64:65], v[50:51] op_sel_hi:[0,1]
	v_pk_mul_f32 v[42:43], v[106:107], v[44:45]
	v_cvt_pk_bf16_f32 v40, v40, v41
	v_pk_mul_f32 v[44:45], v[64:65], v[52:53] op_sel_hi:[0,1]
	v_cvt_pk_fp8_f32 v39, v42, v43 op_sel:[0,0,1]
	v_cvt_pk_bf16_f32 v41, v42, v43
	global_store_dwordx2 v[60:61], v[40:41], off offset:1024
	global_store_dword v[62:63], v39, off offset:512
	v_pk_mul_f32 v[40:41], v[108:109], v[44:45]
	s_nop 0
	v_cvt_pk_fp8_f32 v39, v40, v41
	v_pk_mul_f32 v[44:45], v[64:65], v[54:55] op_sel_hi:[0,1]
	v_pk_mul_f32 v[42:43], v[110:111], v[44:45]
	v_cvt_pk_bf16_f32 v40, v40, v41
	s_nop 0
	v_cvt_pk_fp8_f32 v39, v42, v43 op_sel:[0,0,1]
	v_cvt_pk_bf16_f32 v41, v42, v43
	global_store_dwordx2 v[60:61], v[40:41], off offset:1536
	global_store_dword v[62:63], v39, off offset:768
	v_pk_mul_f32 v[12:13], v[112:113], v[12:13]
	s_nop 0
	v_cvt_pk_fp8_f32 v39, v12, v13
	v_pk_mul_f32 v[14:15], v[114:115], v[14:15]
	v_cvt_pk_bf16_f32 v12, v12, v13
	s_nop 0
	v_cvt_pk_fp8_f32 v39, v14, v15 op_sel:[0,0,1]
	v_cvt_pk_bf16_f32 v13, v14, v15
	global_store_dwordx2 v[60:61], v[12:13], off offset:2048
	global_store_dword v[62:63], v39, off offset:1024
	v_pk_mul_f32 v[8:9], v[116:117], v[8:9]
	s_nop 0
	v_cvt_pk_fp8_f32 v39, v8, v9
	v_pk_mul_f32 v[10:11], v[118:119], v[10:11]
	v_cvt_pk_bf16_f32 v8, v8, v9
	v_cvt_pk_fp8_f32 v39, v10, v11 op_sel:[0,0,1]
	v_cvt_pk_bf16_f32 v9, v10, v11
	global_store_dwordx2 v[60:61], v[8:9], off offset:2560
	global_store_dword v[62:63], v39, off offset:1280
	v_pk_mul_f32 v[4:5], v[120:121], v[4:5]
	s_nop 0
	v_cvt_pk_fp8_f32 v12, v4, v5
	v_pk_mul_f32 v[6:7], v[122:123], v[6:7]
	v_cvt_pk_bf16_f32 v4, v4, v5
	s_nop 0
	v_cvt_pk_fp8_f32 v12, v6, v7 op_sel:[0,0,1]
	v_cvt_pk_bf16_f32 v5, v6, v7
	global_store_dwordx2 v[60:61], v[4:5], off offset:3072
	global_store_dword v[62:63], v12, off offset:1536
	v_pk_mul_f32 v[0:1], v[124:125], v[0:1]
	s_nop 0
	v_cvt_pk_fp8_f32 v65, v0, v1
	v_cvt_pk_bf16_f32 v0, v0, v1
	v_pk_mul_f32 v[2:3], v[64:65], v[2:3] op_sel_hi:[0,1]
	v_pk_mul_f32 v[2:3], v[126:127], v[2:3]
	s_nop 0
	v_cvt_pk_fp8_f32 v65, v2, v3 op_sel:[0,0,1]
	v_cvt_pk_bf16_f32 v1, v2, v3
	global_store_dwordx2 v[60:61], v[0:1], off offset:3584
	global_store_dword v[62:63], v65, off offset:1792
	s_cbranch_scc0 .LBB0_46
